# P4 pass loops: next key fragments loaded straight into v128-143 (the registers the next iteration reads) - removes 16 v_mov_b64 copies and the back-edge vmcnt(0) per two tiles
# baseline (speedup 1.0000x reference)
; __device__ __forceinline__ int crow(int reg, int h) { return (reg & 3) + 8 * (reg >> 2) + 4 * h; }
; template <int STAGE>
; __device__ __forceinline__ void pass2(LAS unsigned char* lds, const bf16* kbase, int g, int t0, const bf16x8 (&qf)[4][4], const f32x4 lo4, const f32x4 hi4, int wave, int r, int h2) {
;     ...
;         f32x16 acc[4];
; #pragma unroll
;         for (int hd = 0; hd < 4; ++hd) {
;             acc[hd] = f32x16{};
; #pragma unroll
;             for (int s = 0; s < 4; ++s) acc[hd] = __builtin_amdgcn_mfma_f32_32x32x16_bf16(WN ? kn[s] : kf[s], qf[hd][s], acc[hd], 0, 0, 0);
;         }
;         const int zi = (8191 - 32 * kt) >> 7;
;         const int lim = tq - 32 * kt - 4 * h2;
;         unsigned gtw = 0u, eqw = 0u;
;         float svq[16];
; #pragma unroll
;         for (int rg = 0; rg < 16; ++rg) {
;             const int c0 = att::crow(rg, 0);
;             float sv = fsum4_s(__builtin_amdgcn_fmed3f(acc[0][rg], lo4.x, hi4.x), __builtin_amdgcn_fmed3f(acc[1][rg], lo4.y, hi4.y),
;                                __builtin_amdgcn_fmed3f(acc[2][rg], lo4.z, hi4.z), __builtin_amdgcn_fmed3f(acc[3][rg], lo4.w, hi4.w));
;             const int b = bin2(sv, zi);
;             const bool valid = !DIAG || c0 <= lim;
;             if (STAGE == 0) {
;                 atomicAdd((unsigned*)&hist[r * HROW2 + (valid ? b : NB2)], 1u);
.LBB0_787:
	s_add_i32 s4, s0, s1
	s_cmp_lg_u32 s4, 16
	s_cbranch_scc0 .LBB0_793
	s_waitcnt vmcnt(3)
	v_mfma_f32_32x32x16_bf16 v[0:15], v[140:143], v[64:67], 0
	s_lshr_b32 s4, s6, 7
	s_addk_i32 s4, 0xd0
	v_mfma_f32_32x32x16_bf16 v[16:31], v[140:143], v[80:83], 0
	v_mfma_f32_32x32x16_bf16 v[32:47], v[140:143], v[96:99], 0
	v_mfma_f32_32x32x16_bf16 v[48:63], v[140:143], v[112:115], 0
	s_waitcnt vmcnt(2)
	v_mfma_f32_32x32x16_bf16 v[0:15], v[136:139], v[68:71], v[0:15]
	v_mfma_f32_32x32x16_bf16 v[16:31], v[136:139], v[84:87], v[16:31]
	v_mfma_f32_32x32x16_bf16 v[32:47], v[136:139], v[100:103], v[32:47]
	v_mfma_f32_32x32x16_bf16 v[48:63], v[136:139], v[116:119], v[48:63]
	s_waitcnt vmcnt(1)
	v_mfma_f32_32x32x16_bf16 v[0:15], v[132:135], v[72:75], v[0:15]
	v_mfma_f32_32x32x16_bf16 v[16:31], v[132:135], v[88:91], v[16:31]
	v_mfma_f32_32x32x16_bf16 v[32:47], v[132:135], v[104:107], v[32:47]
	v_mfma_f32_32x32x16_bf16 v[48:63], v[132:135], v[120:123], v[48:63]
	s_waitcnt vmcnt(0)
	v_mfma_f32_32x32x16_bf16 v[0:15], v[128:131], v[76:79], v[0:15]
	v_mfma_f32_32x32x16_bf16 v[16:31], v[128:131], v[92:95], v[16:31]
	s_nop 10
	v_med3_f32 v0, v0, v207, v208
	v_mfma_f32_32x32x16_bf16 v[32:47], v[128:131], v[108:111], v[32:47]
	v_med3_f32 v16, v16, v209, v210
	v_mfma_f32_32x32x16_bf16 v[48:63], v[128:131], v[124:127], v[48:63]
	s_nop 9
	v_med3_f32 v32, v32, v212, v213
	s_nop 0
	v_med3_f32 v48, v48, v214, v215
	v_add_f32 v160, v0, v16
	v_add_f32 v161, v32, v48
	v_add_f32 v160, v160, v161
	v_med3_f32 v32, v49, v214, v215
	v_bfe_u32 v0, v160, 20, 11
	v_med3_u32 v0, v0, s91, v190
	v_sub_u32_e32 v16, 0x40f, v0
	v_add_u32_e32 v0, 0xfffffdd0, v0
	v_cmp_gt_i32_e32 vcc, 0, v160
	s_nop 1
	v_cndmask_b32_e32 v0, v0, v16, vcc
	v_mov_b32_e32 v16, s4
	v_cmp_eq_f32_e32 vcc, 0, v160
	s_mov_b64 s[4:5], -1
	s_nop 0
	v_cndmask_b32_e32 v0, v0, v16, vcc
	v_lshl_add_u32 v0, v0, 2, v204
	ds_add_u32 v0, v184
	v_med3_f32 v0, v1, v207, v208
	v_med3_f32 v1, v17, v209, v210
	v_med3_f32 v17, v33, v212, v213
	v_add_f32 v33, v0, v1
	v_add_f32 v48, v17, v32
	v_add_f32 v33, v33, v48
	v_med3_f32 v17, v50, v214, v215
	v_bfe_u32 v0, v33, 20, 11
	v_med3_u32 v0, v0, s91, v190
	v_sub_u32_e32 v1, 0x40f, v0
	v_add_u32_e32 v0, 0xfffffdd0, v0
	v_cmp_gt_i32_e64 s[98:99], 0, v33
	v_cmp_eq_f32_e32 vcc, 0, v33
	s_nop 0
	v_cndmask_b32_e64 v0, v0, v1, s[98:99]
	v_med3_f32 v1, v18, v209, v210
	v_cndmask_b32_e32 v0, v0, v16, vcc
	v_lshl_add_u32 v0, v0, 2, v204
	ds_add_u32 v0, v184
	v_med3_f32 v0, v2, v207, v208
	v_med3_f32 v2, v34, v212, v213
	v_add_f32 v18, v0, v1
	v_add_f32 v32, v2, v17
	v_add_f32 v18, v18, v32
	v_med3_f32 v2, v35, v212, v213
	v_bfe_u32 v0, v18, 20, 11
	v_med3_u32 v0, v0, s91, v190
	v_sub_u32_e32 v1, 0x40f, v0
	v_add_u32_e32 v0, 0xfffffdd0, v0
	v_cmp_gt_i32_e64 s[98:99], 0, v18
	v_cmp_eq_f32_e32 vcc, 0, v18
	s_nop 0
	v_cndmask_b32_e64 v0, v0, v1, s[98:99]
	v_med3_f32 v1, v19, v209, v210
	v_cndmask_b32_e32 v0, v0, v16, vcc
	v_lshl_add_u32 v0, v0, 2, v204
	ds_add_u32 v0, v184
	v_med3_f32 v0, v3, v207, v208
	v_med3_f32 v3, v51, v214, v215
	v_add_f32 v17, v0, v1
	v_add_f32 v18, v2, v3
	v_add_f32 v17, v17, v18
	v_med3_f32 v2, v36, v212, v213
	v_bfe_u32 v0, v17, 20, 11
	v_med3_u32 v0, v0, s91, v190
	v_sub_u32_e32 v1, 0x40f, v0
	v_add_u32_e32 v0, 0xfffffdd0, v0
	v_cmp_gt_i32_e64 s[98:99], 0, v17
	v_cmp_eq_f32_e32 vcc, 0, v17
	v_med3_f32 v3, v52, v214, v215
	v_cndmask_b32_e64 v0, v0, v1, s[98:99]
	v_med3_f32 v1, v20, v209, v210
	v_cndmask_b32_e32 v0, v0, v16, vcc
	v_lshl_add_u32 v0, v0, 2, v204
	ds_add_u32 v0, v184
	v_med3_f32 v0, v4, v207, v208
	v_add_f32 v4, v0, v1
	v_add_f32 v17, v2, v3
	v_add_f32 v4, v4, v17
	v_med3_f32 v2, v37, v212, v213
	v_bfe_u32 v0, v4, 20, 11
	v_med3_u32 v0, v0, s91, v190
	v_sub_u32_e32 v1, 0x40f, v0
	v_add_u32_e32 v0, 0xfffffdd0, v0
	v_cmp_gt_i32_e64 s[98:99], 0, v4
	v_cmp_eq_f32_e32 vcc, 0, v4
	v_med3_f32 v3, v53, v214, v215
	v_cndmask_b32_e64 v0, v0, v1, s[98:99]
	v_med3_f32 v1, v21, v209, v210
	v_cndmask_b32_e32 v0, v0, v16, vcc
	v_lshl_add_u32 v0, v0, 2, v204
	ds_add_u32 v0, v184
	v_med3_f32 v0, v5, v207, v208
	v_add_f32 v4, v0, v1
	v_add_f32 v5, v2, v3
	v_add_f32 v4, v4, v5
	v_med3_f32 v2, v38, v212, v213
	v_bfe_u32 v0, v4, 20, 11
	v_med3_u32 v0, v0, s91, v190
	v_sub_u32_e32 v1, 0x40f, v0
	v_add_u32_e32 v0, 0xfffffdd0, v0
	v_cmp_gt_i32_e64 s[98:99], 0, v4
	v_cmp_eq_f32_e32 vcc, 0, v4
	v_med3_f32 v3, v54, v214, v215
	v_cndmask_b32_e64 v0, v0, v1, s[98:99]
	v_med3_f32 v1, v22, v209, v210
	v_cndmask_b32_e32 v0, v0, v16, vcc
	v_lshl_add_u32 v0, v0, 2, v204
	ds_add_u32 v0, v184
	v_med3_f32 v0, v6, v207, v208
	v_add_f32 v4, v0, v1
	v_add_f32 v5, v2, v3
	v_add_f32 v4, v4, v5
	v_med3_f32 v2, v39, v212, v213
	v_bfe_u32 v0, v4, 20, 11
	v_med3_u32 v0, v0, s91, v190
	v_sub_u32_e32 v1, 0x40f, v0
	v_add_u32_e32 v0, 0xfffffdd0, v0
	v_cmp_gt_i32_e64 s[98:99], 0, v4
	v_cmp_eq_f32_e32 vcc, 0, v4
	v_med3_f32 v3, v55, v214, v215
	v_cndmask_b32_e64 v0, v0, v1, s[98:99]
	v_med3_f32 v1, v23, v209, v210
; __device__ __forceinline__ int crow(int reg, int h) { return (reg & 3) + 8 * (reg >> 2) + 4 * h; }
; #define DSA2_LOADK(dst, kt_) do { _Pragma("unroll") for (int s = 0; s < 4; ++s) dst[s] = *(const bf16x8*)(kp + (size_t)(32 * (kt_)) * Y0P + 16 * s); } while (0)
; template <int STAGE>
; __device__ __forceinline__ void pass2(LAS unsigned char* lds, const bf16* kbase, int g, int t0, const bf16x8 (&qf)[4][4], const f32x4 lo4, const f32x4 hi4, int wave, int r, int h2) {
;     ...
;         for (int rg = 0; rg < 16; ++rg) {
;             const int c0 = att::crow(rg, 0);
;             float sv = fsum4_s(__builtin_amdgcn_fmed3f(acc[0][rg], lo4.x, hi4.x), __builtin_amdgcn_fmed3f(acc[1][rg], lo4.y, hi4.y),
;                                __builtin_amdgcn_fmed3f(acc[2][rg], lo4.z, hi4.z), __builtin_amdgcn_fmed3f(acc[3][rg], lo4.w, hi4.w));
;             const int b = bin2(sv, zi);
;             const bool valid = !DIAG || c0 <= lim;
;             if (STAGE == 0) {
;                 atomicAdd((unsigned*)&hist[r * HROW2 + (valid ? b : NB2)], 1u);
;     ...
;         kt += 8;
;         if (kt > g) break;
;         if (kt + 8 <= g) DSA2_LOADK(kf, kt + 8);
	v_cndmask_b32_e32 v0, v0, v16, vcc
	v_lshl_add_u32 v0, v0, 2, v204
	ds_add_u32 v0, v184
	v_med3_f32 v0, v7, v207, v208
	v_add_f32 v4, v0, v1
	v_add_f32 v5, v2, v3
	v_add_f32 v4, v4, v5
	v_med3_f32 v2, v40, v212, v213
	v_bfe_u32 v0, v4, 20, 11
	v_med3_u32 v0, v0, s91, v190
	v_sub_u32_e32 v1, 0x40f, v0
	v_add_u32_e32 v0, 0xfffffdd0, v0
	v_cmp_gt_i32_e64 s[98:99], 0, v4
	v_cmp_eq_f32_e32 vcc, 0, v4
	v_med3_f32 v3, v56, v214, v215
	v_cndmask_b32_e64 v0, v0, v1, s[98:99]
	v_med3_f32 v1, v24, v209, v210
	v_cndmask_b32_e32 v0, v0, v16, vcc
	v_lshl_add_u32 v0, v0, 2, v204
	ds_add_u32 v0, v184
	v_med3_f32 v0, v8, v207, v208
	v_add_f32 v4, v0, v1
	v_add_f32 v5, v2, v3
	v_add_f32 v4, v4, v5
	v_med3_f32 v2, v41, v212, v213
	v_bfe_u32 v0, v4, 20, 11
	v_med3_u32 v0, v0, s91, v190
	v_sub_u32_e32 v1, 0x40f, v0
	v_add_u32_e32 v0, 0xfffffdd0, v0
	v_cmp_gt_i32_e64 s[98:99], 0, v4
	v_cmp_eq_f32_e32 vcc, 0, v4
	v_med3_f32 v3, v57, v214, v215
	v_cndmask_b32_e64 v0, v0, v1, s[98:99]
	v_med3_f32 v1, v25, v209, v210
	v_cndmask_b32_e32 v0, v0, v16, vcc
	v_lshl_add_u32 v0, v0, 2, v204
	ds_add_u32 v0, v184
	v_med3_f32 v0, v9, v207, v208
	v_add_f32 v4, v0, v1
	v_add_f32 v5, v2, v3
	v_add_f32 v4, v4, v5
	v_med3_f32 v2, v42, v212, v213
	v_bfe_u32 v0, v4, 20, 11
	v_med3_u32 v0, v0, s91, v190
	v_sub_u32_e32 v1, 0x40f, v0
	v_add_u32_e32 v0, 0xfffffdd0, v0
	v_cmp_gt_i32_e64 s[98:99], 0, v4
	v_cmp_eq_f32_e32 vcc, 0, v4
	v_med3_f32 v3, v58, v214, v215
	v_cndmask_b32_e64 v0, v0, v1, s[98:99]
	v_med3_f32 v1, v26, v209, v210
	v_cndmask_b32_e32 v0, v0, v16, vcc
	v_lshl_add_u32 v0, v0, 2, v204
	ds_add_u32 v0, v184
	v_med3_f32 v0, v10, v207, v208
	v_add_f32 v4, v0, v1
	v_add_f32 v5, v2, v3
	v_add_f32 v4, v4, v5
	v_med3_f32 v2, v43, v212, v213
	v_bfe_u32 v0, v4, 20, 11
	v_med3_u32 v0, v0, s91, v190
	v_sub_u32_e32 v1, 0x40f, v0
	v_add_u32_e32 v0, 0xfffffdd0, v0
	v_cmp_gt_i32_e64 s[98:99], 0, v4
	v_cmp_eq_f32_e32 vcc, 0, v4
	v_med3_f32 v3, v59, v214, v215
	v_cndmask_b32_e64 v0, v0, v1, s[98:99]
	v_med3_f32 v1, v27, v209, v210
	v_cndmask_b32_e32 v0, v0, v16, vcc
	v_lshl_add_u32 v0, v0, 2, v204
	ds_add_u32 v0, v184
	v_med3_f32 v0, v11, v207, v208
	v_add_f32 v4, v0, v1
	v_add_f32 v5, v2, v3
	v_add_f32 v4, v4, v5
	v_med3_f32 v2, v44, v212, v213
	v_bfe_u32 v0, v4, 20, 11
	v_med3_u32 v0, v0, s91, v190
	v_sub_u32_e32 v1, 0x40f, v0
	v_add_u32_e32 v0, 0xfffffdd0, v0
	v_cmp_gt_i32_e64 s[98:99], 0, v4
	v_cmp_eq_f32_e32 vcc, 0, v4
	v_med3_f32 v3, v60, v214, v215
	v_cndmask_b32_e64 v0, v0, v1, s[98:99]
	v_med3_f32 v1, v28, v209, v210
	v_cndmask_b32_e32 v0, v0, v16, vcc
	v_lshl_add_u32 v0, v0, 2, v204
	ds_add_u32 v0, v184
	v_med3_f32 v0, v12, v207, v208
	v_add_f32 v4, v0, v1
	v_add_f32 v5, v2, v3
	v_add_f32 v4, v4, v5
	v_med3_f32 v2, v45, v212, v213
	v_bfe_u32 v0, v4, 20, 11
	v_med3_u32 v0, v0, s91, v190
	v_sub_u32_e32 v1, 0x40f, v0
	v_add_u32_e32 v0, 0xfffffdd0, v0
	v_cmp_gt_i32_e64 s[98:99], 0, v4
	v_cmp_eq_f32_e32 vcc, 0, v4
	v_med3_f32 v3, v61, v214, v215
	v_cndmask_b32_e64 v0, v0, v1, s[98:99]
	v_med3_f32 v1, v29, v209, v210
	v_cndmask_b32_e32 v0, v0, v16, vcc
	v_lshl_add_u32 v0, v0, 2, v204
	ds_add_u32 v0, v184
	v_med3_f32 v0, v13, v207, v208
	v_add_f32 v4, v0, v1
	v_add_f32 v5, v2, v3
	v_add_f32 v4, v4, v5
	v_med3_f32 v2, v46, v212, v213
	v_bfe_u32 v0, v4, 20, 11
	v_med3_u32 v0, v0, s91, v190
	v_sub_u32_e32 v1, 0x40f, v0
	v_add_u32_e32 v0, 0xfffffdd0, v0
	v_cmp_gt_i32_e64 s[98:99], 0, v4
	v_cmp_eq_f32_e32 vcc, 0, v4
	v_med3_f32 v3, v62, v214, v215
	v_cndmask_b32_e64 v0, v0, v1, s[98:99]
	v_med3_f32 v1, v30, v209, v210
	v_cndmask_b32_e32 v0, v0, v16, vcc
	v_lshl_add_u32 v0, v0, 2, v204
	ds_add_u32 v0, v184
	v_med3_f32 v0, v14, v207, v208
	v_add_f32 v4, v0, v1
	v_add_f32 v5, v2, v3
	v_add_f32 v4, v4, v5
	v_med3_f32 v2, v47, v212, v213
	v_bfe_u32 v0, v4, 20, 11
	v_med3_u32 v0, v0, s91, v190
	v_sub_u32_e32 v1, 0x40f, v0
	v_add_u32_e32 v0, 0xfffffdd0, v0
	v_cmp_gt_i32_e64 s[98:99], 0, v4
	v_cmp_eq_f32_e32 vcc, 0, v4
	v_med3_f32 v3, v63, v214, v215
	v_cndmask_b32_e64 v0, v0, v1, s[98:99]
	v_med3_f32 v1, v31, v209, v210
	v_cndmask_b32_e32 v0, v0, v16, vcc
	v_lshl_add_u32 v0, v0, 2, v204
	ds_add_u32 v0, v184
	v_med3_f32 v0, v15, v207, v208
	v_add_f32 v4, v0, v1
	v_add_f32 v5, v2, v3
	v_add_f32 v4, v4, v5
	s_nop 0
	v_bfe_u32 v0, v4, 20, 11
	v_med3_u32 v0, v0, s91, v190
	v_sub_u32_e32 v1, 0x40f, v0
	v_add_u32_e32 v0, 0xfffffdd0, v0
	v_cmp_gt_i32_e64 s[98:99], 0, v4
	v_cmp_eq_f32_e32 vcc, 0, v4
	s_nop 0
	v_cndmask_b32_e64 v0, v0, v1, s[98:99]
	v_cndmask_b32_e32 v0, v0, v16, vcc
	v_lshl_add_u32 v0, v0, 2, v204
	ds_add_u32 v0, v184
	s_and_b64 vcc, exec, s[2:3]
	s_mov_b64 s[2:3], -1
	s_cbranch_vccz .LBB0_794
	s_cmp_gt_u32 s1, s64
	s_cselect_b64 s[2:3], -1, 0
	s_and_b64 vcc, exec, s[2:3]
	s_cbranch_vccnz .LBB0_791
	global_load_dwordx4 v[140:143], v[180:181], off offset:-96
	global_load_dwordx4 v[136:139], v[180:181], off offset:-64
	global_load_dwordx4 v[132:135], v[180:181], off offset:-32
	global_load_dwordx4 v[128:131], v[180:181], off

; __device__ __forceinline__ int crow(int reg, int h) { return (reg & 3) + 8 * (reg >> 2) + 4 * h; }
; #define DSA2_LOADK(dst, kt_) do { _Pragma("unroll") for (int s = 0; s < 4; ++s) dst[s] = *(const bf16x8*)(kp + (size_t)(32 * (kt_)) * Y0P + 16 * s); } while (0)
; template <int STAGE>
; __device__ __forceinline__ void pass2(LAS unsigned char* lds, const bf16* kbase, int g, int t0, const bf16x8 (&qf)[4][4], const f32x4 lo4, const f32x4 hi4, int wave, int r, int h2) {
;     ...
;         f32x16 acc[4];
; #pragma unroll
;         for (int hd = 0; hd < 4; ++hd) {
;             acc[hd] = f32x16{};
; #pragma unroll
;             for (int s = 0; s < 4; ++s) acc[hd] = __builtin_amdgcn_mfma_f32_32x32x16_bf16(WN ? kn[s] : kf[s], qf[hd][s], acc[hd], 0, 0, 0);
;         }
;         const int zi = (8191 - 32 * kt) >> 7;
;         const int lim = tq - 32 * kt - 4 * h2;
;         unsigned gtw = 0u, eqw = 0u;
;         float svq[16];
; #pragma unroll
;         for (int rg = 0; rg < 16; ++rg) {
;             const int c0 = att::crow(rg, 0);
;             float sv = fsum4_s(__builtin_amdgcn_fmed3f(acc[0][rg], lo4.x, hi4.x), __builtin_amdgcn_fmed3f(acc[1][rg], lo4.y, hi4.y),
;                                __builtin_amdgcn_fmed3f(acc[2][rg], lo4.z, hi4.z), __builtin_amdgcn_fmed3f(acc[3][rg], lo4.w, hi4.w));
;             const int b = bin2(sv, zi);
;             const bool valid = !DIAG || c0 <= lim;
;             if (STAGE == 0) {
;                 atomicAdd((unsigned*)&hist[r * HROW2 + (valid ? b : NB2)], 1u);
;     ...
;         kt += 8;
;         if (kt > g) break;
;         if (kt + 8 <= g) DSA2_LOADK(kf, kt + 8);
;         if (kt == g) { tile(pg8::BoolC2<true>{}, kt, pg8::BoolC2<true>{}); break; }
;         tile(pg8::BoolC2<true>{}, kt, pg8::BoolC2<false>{});
;         kt += 8;
;     }
.LBB0_795:
	s_mov_b64 s[4:5], 0
	s_mov_b64 s[8:9], 0
	s_cbranch_execnz .LBB0_797
.LBB0_796:
	s_branch .LBB0_785
.LBB0_797:
	s_mov_b64 s[2:3], -1
	s_mov_b64 s[6:7], 0
	s_and_b64 vcc, exec, s[8:9]
	s_cbranch_vccnz .LBB0_800
	s_xor_b64 s[0:1], s[4:5], -1
	s_mov_b64 s[2:3], 0
	s_and_b64 vcc, exec, s[0:1]
	s_cbranch_vccz .LBB0_800
	s_waitcnt vmcnt(3)
	v_mfma_f32_32x32x16_bf16 v[0:15], v[156:159], v[64:67], 0
	s_lshr_b32 s0, s64, 2
	s_sub_i32 s0, 0x10f, s0
	s_mov_b64 s[6:7], -1
	v_mfma_f32_32x32x16_bf16 v[16:31], v[156:159], v[80:83], 0
	v_mfma_f32_32x32x16_bf16 v[32:47], v[156:159], v[96:99], 0
	v_mfma_f32_32x32x16_bf16 v[48:63], v[156:159], v[112:115], 0
	s_waitcnt vmcnt(2)
	v_mfma_f32_32x32x16_bf16 v[0:15], v[152:155], v[68:71], v[0:15]
	v_mfma_f32_32x32x16_bf16 v[16:31], v[152:155], v[84:87], v[16:31]
	v_mfma_f32_32x32x16_bf16 v[32:47], v[152:155], v[100:103], v[32:47]
	v_mfma_f32_32x32x16_bf16 v[48:63], v[152:155], v[116:119], v[48:63]
	s_waitcnt vmcnt(1)
	v_mfma_f32_32x32x16_bf16 v[0:15], v[148:151], v[72:75], v[0:15]
	v_mfma_f32_32x32x16_bf16 v[16:31], v[148:151], v[88:91], v[16:31]
	v_mfma_f32_32x32x16_bf16 v[32:47], v[148:151], v[104:107], v[32:47]
	v_mfma_f32_32x32x16_bf16 v[48:63], v[148:151], v[120:123], v[48:63]
	v_lshlrev_b32_e32 v148, 2, v219
	v_sub_u32_e32 v160, v218, v148
	s_waitcnt vmcnt(0)
	v_mfma_f32_32x32x16_bf16 v[0:15], v[144:147], v[76:79], v[0:15]
	v_mfma_f32_32x32x16_bf16 v[16:31], v[144:147], v[92:95], v[16:31]
	s_nop 10
	v_med3_f32 v0, v0, v207, v208
	v_med3_f32 v1, v1, v207, v208
	v_mfma_f32_32x32x16_bf16 v[32:47], v[144:147], v[108:111], v[32:47]
	v_med3_f32 v16, v16, v209, v210
	v_mfma_f32_32x32x16_bf16 v[48:63], v[144:147], v[124:127], v[48:63]
	s_nop 9
	v_med3_f32 v32, v32, v212, v213
	s_nop 0
	v_med3_f32 v48, v48, v214, v215
	v_add_f32 v144, v0, v16
	v_add_f32 v145, v32, v48
	v_add_f32 v144, v144, v145
	v_med3_f32 v32, v49, v214, v215
	v_bfe_u32 v0, v144, 20, 11
	v_med3_u32 v0, v0, s91, v190
	v_sub_u32_e32 v16, 0x40f, v0
	v_add_u32_e32 v0, 0xfffffdd0, v0
	v_cmp_gt_i32_e32 vcc, 0, v144
	s_nop 1
	v_cndmask_b32_e32 v16, v0, v16, vcc
	v_mov_b32_e32 v0, s0
	v_cmp_eq_f32_e32 vcc, 0, v144
	s_nop 1
	v_cndmask_b32_e32 v16, v16, v0, vcc
	v_cmp_lt_i32_e32 vcc, -1, v160
	s_nop 1
	v_cndmask_b32_e32 v16, v191, v16, vcc
	v_lshl_add_u32 v16, v16, 2, v204
	ds_add_u32 v16, v184
	v_med3_f32 v16, v17, v209, v210
	v_med3_f32 v17, v33, v212, v213
	v_add_f32 v33, v1, v16
	v_add_f32 v48, v17, v32
	v_add_f32 v33, v33, v48
	v_med3_f32 v17, v50, v214, v215
	v_bfe_u32 v1, v33, 20, 11
	v_med3_u32 v1, v1, s91, v190
	v_sub_u32_e32 v16, 0x40f, v1
	v_add_u32_e32 v1, 0xfffffdd0, v1
	v_cmp_gt_i32_e32 vcc, 0, v33
	s_nop 1
	v_cndmask_b32_e32 v1, v1, v16, vcc
	v_cmp_eq_f32_e32 vcc, 0, v33
	v_med3_f32 v16, v34, v212, v213
	s_nop 0
	v_cndmask_b32_e32 v1, v1, v0, vcc
	v_cmp_lt_i32_e32 vcc, 0, v160
	s_nop 1
	v_cndmask_b32_e32 v1, v191, v1, vcc
	v_lshl_add_u32 v1, v1, 2, v204
	ds_add_u32 v1, v184
	v_med3_f32 v1, v2, v207, v208
	v_med3_f32 v2, v18, v209, v210
	v_add_f32 v18, v1, v2
	v_add_f32 v32, v16, v17
	v_add_f32 v18, v18, v32
	v_med3_f32 v16, v51, v214, v215
	v_bfe_u32 v1, v18, 20, 11
	v_med3_u32 v1, v1, s91, v190
	v_sub_u32_e32 v2, 0x40f, v1
	v_add_u32_e32 v1, 0xfffffdd0, v1
	v_cmp_gt_i32_e32 vcc, 0, v18
	s_nop 1
	v_cndmask_b32_e32 v1, v1, v2, vcc
	v_cmp_eq_f32_e32 vcc, 0, v18
	v_med3_f32 v2, v19, v209, v210
	s_nop 0
	v_cndmask_b32_e32 v1, v1, v0, vcc
	v_cmp_lt_i32_e32 vcc, 1, v160
	s_nop 1
	v_cndmask_b32_e32 v1, v191, v1, vcc
	v_lshl_add_u32 v1, v1, 2, v204
	ds_add_u32 v1, v184
	v_med3_f32 v1, v3, v207, v208
	v_med3_f32 v3, v35, v212, v213
	v_add_f32 v17, v1, v2
	v_add_f32 v18, v3, v16
	v_add_f32 v17, v17, v18
	v_med3_f32 v3, v36, v212, v213
	v_bfe_u32 v1, v17, 20, 11
	v_med3_u32 v1, v1, s91, v190
	v_sub_u32_e32 v2, 0x40f, v1
	v_add_u32_e32 v1, 0xfffffdd0, v1
	v_cmp_gt_i32_e32 vcc, 0, v17
	s_nop 1
	v_cndmask_b32_e32 v1, v1, v2, vcc
	v_cmp_eq_f32_e32 vcc, 0, v17
	v_med3_f32 v2, v20, v209, v210
	s_nop 0
	v_cndmask_b32_e32 v1, v1, v0, vcc
	v_cmp_lt_i32_e32 vcc, 2, v160
	s_nop 1
	v_cndmask_b32_e32 v1, v191, v1, vcc
	v_lshl_add_u32 v1, v1, 2, v204
	ds_add_u32 v1, v184
	v_med3_f32 v1, v4, v207, v208
	v_med3_f32 v4, v52, v214, v215
	v_add_f32 v16, v1, v2
	v_add_f32 v17, v3, v4
	v_add_f32 v16, v16, v17
	v_med3_f32 v3, v37, v212, v213
	v_bfe_u32 v1, v16, 20, 11
	v_med3_u32 v1, v1, s91, v190
	v_sub_u32_e32 v2, 0x40f, v1
	v_add_u32_e32 v1, 0xfffffdd0, v1
	v_cmp_gt_i32_e32 vcc, 0, v16
	v_med3_f32 v4, v53, v214, v215
	s_nop 0
	v_cndmask_b32_e32 v1, v1, v2, vcc
	v_cmp_eq_f32_e32 vcc, 0, v16
	v_med3_f32 v2, v21, v209, v210
	s_nop 0
	v_cndmask_b32_e32 v1, v1, v0, vcc
	v_cmp_lt_i32_e32 vcc, 7, v160
	s_nop 1
	v_cndmask_b32_e32 v1, v191, v1, vcc
	v_lshl_add_u32 v1, v1, 2, v204
	ds_add_u32 v1, v184
	v_med3_f32 v1, v5, v207, v208
	v_add_f32 v5, v1, v2
	v_add_f32 v16, v3, v4
	v_add_f32 v5, v5, v16
	v_med3_f32 v3, v38, v212, v213
	v_bfe_u32 v1, v5, 20, 11
	v_med3_u32 v1, v1, s91, v190
	v_sub_u32_e32 v2, 0x40f, v1
	v_add_u32_e32 v1, 0xfffffdd0, v1
	v_cmp_gt_i32_e32 vcc, 0, v5
	v_med3_f32 v4, v54, v214, v215
	s_nop 0
	v_cndmask_b32_e32 v1, v1, v2, vcc
	v_cmp_eq_f32_e32 vcc, 0, v5
	v_med3_f32 v2, v22, v209, v210
	s_nop 0
	v_cndmask_b32_e32 v1, v1, v0, vcc
	v_cmp_lt_i32_e32 vcc, 8, v160
	s_nop 1
	v_cndmask_b32_e32 v1, v191, v1, vcc
	v_lshl_add_u32 v1, v1, 2, v204
	ds_add_u32 v1, v184
	v_med3_f32 v1, v6, v207, v208
; __device__ __forceinline__ int crow(int reg, int h) { return (reg & 3) + 8 * (reg >> 2) + 4 * h; }
; template <int STAGE>
; __device__ __forceinline__ void pass2(LAS unsigned char* lds, const bf16* kbase, int g, int t0, const bf16x8 (&qf)[4][4], const f32x4 lo4, const f32x4 hi4, int wave, int r, int h2) {
;     ...
;         for (int rg = 0; rg < 16; ++rg) {
;             const int c0 = att::crow(rg, 0);
;             float sv = fsum4_s(__builtin_amdgcn_fmed3f(acc[0][rg], lo4.x, hi4.x), __builtin_amdgcn_fmed3f(acc[1][rg], lo4.y, hi4.y),
;                                __builtin_amdgcn_fmed3f(acc[2][rg], lo4.z, hi4.z), __builtin_amdgcn_fmed3f(acc[3][rg], lo4.w, hi4.w));
;             const int b = bin2(sv, zi);
;             const bool valid = !DIAG || c0 <= lim;
;             if (STAGE == 0) {
;                 atomicAdd((unsigned*)&hist[r * HROW2 + (valid ? b : NB2)], 1u);
	v_add_f32 v5, v1, v2
	v_add_f32 v6, v3, v4
	v_add_f32 v5, v5, v6
	v_med3_f32 v3, v39, v212, v213
	v_bfe_u32 v1, v5, 20, 11
	v_med3_u32 v1, v1, s91, v190
	v_sub_u32_e32 v2, 0x40f, v1
	v_add_u32_e32 v1, 0xfffffdd0, v1
	v_cmp_gt_i32_e32 vcc, 0, v5
	v_med3_f32 v4, v55, v214, v215
	s_nop 0
	v_cndmask_b32_e32 v1, v1, v2, vcc
	v_cmp_eq_f32_e32 vcc, 0, v5
	v_med3_f32 v2, v23, v209, v210
	s_nop 0
	v_cndmask_b32_e32 v1, v1, v0, vcc
	v_cmp_lt_i32_e32 vcc, 9, v160
	s_nop 1
	v_cndmask_b32_e32 v1, v191, v1, vcc
	v_lshl_add_u32 v1, v1, 2, v204
	ds_add_u32 v1, v184
	v_med3_f32 v1, v7, v207, v208
	v_add_f32 v5, v1, v2
	v_add_f32 v6, v3, v4
	v_add_f32 v5, v5, v6
	v_med3_f32 v3, v40, v212, v213
	v_bfe_u32 v1, v5, 20, 11
	v_med3_u32 v1, v1, s91, v190
	v_sub_u32_e32 v2, 0x40f, v1
	v_add_u32_e32 v1, 0xfffffdd0, v1
	v_cmp_gt_i32_e32 vcc, 0, v5
	v_med3_f32 v4, v56, v214, v215
	s_nop 0
	v_cndmask_b32_e32 v1, v1, v2, vcc
	v_cmp_eq_f32_e32 vcc, 0, v5
	v_med3_f32 v2, v24, v209, v210
	s_nop 0
	v_cndmask_b32_e32 v1, v1, v0, vcc
	v_cmp_lt_i32_e32 vcc, 10, v160
	s_nop 1
	v_cndmask_b32_e32 v1, v191, v1, vcc
	v_lshl_add_u32 v1, v1, 2, v204
	ds_add_u32 v1, v184
	v_med3_f32 v1, v8, v207, v208
	v_add_f32 v5, v1, v2
	v_add_f32 v6, v3, v4
	v_add_f32 v5, v5, v6
	v_med3_f32 v3, v41, v212, v213
	v_bfe_u32 v1, v5, 20, 11
	v_med3_u32 v1, v1, s91, v190
	v_sub_u32_e32 v2, 0x40f, v1
	v_add_u32_e32 v1, 0xfffffdd0, v1
	v_cmp_gt_i32_e32 vcc, 0, v5
	v_med3_f32 v4, v57, v214, v215
	s_nop 0
	v_cndmask_b32_e32 v1, v1, v2, vcc
	v_cmp_eq_f32_e32 vcc, 0, v5
	v_med3_f32 v2, v25, v209, v210
	s_nop 0
	v_cndmask_b32_e32 v1, v1, v0, vcc
	v_cmp_lt_i32_e32 vcc, 15, v160
	s_nop 1
	v_cndmask_b32_e32 v1, v191, v1, vcc
	v_lshl_add_u32 v1, v1, 2, v204
	ds_add_u32 v1, v184
	v_med3_f32 v1, v9, v207, v208
	v_add_f32 v5, v1, v2
	v_add_f32 v6, v3, v4
	v_add_f32 v5, v5, v6
	v_med3_f32 v3, v42, v212, v213
	v_bfe_u32 v1, v5, 20, 11
	v_med3_u32 v1, v1, s91, v190
	v_sub_u32_e32 v2, 0x40f, v1
	v_add_u32_e32 v1, 0xfffffdd0, v1
	v_cmp_gt_i32_e32 vcc, 0, v5
	v_med3_f32 v4, v58, v214, v215
	s_nop 0
	v_cndmask_b32_e32 v1, v1, v2, vcc
	v_cmp_eq_f32_e32 vcc, 0, v5
	v_med3_f32 v2, v26, v209, v210
	s_nop 0
	v_cndmask_b32_e32 v1, v1, v0, vcc
	v_cmp_lt_i32_e32 vcc, 16, v160
	s_nop 1
	v_cndmask_b32_e32 v1, v191, v1, vcc
	v_lshl_add_u32 v1, v1, 2, v204
	ds_add_u32 v1, v184
	v_med3_f32 v1, v10, v207, v208
	v_add_f32 v5, v1, v2
	v_add_f32 v6, v3, v4
	v_add_f32 v5, v5, v6
	v_med3_f32 v3, v43, v212, v213
	v_bfe_u32 v1, v5, 20, 11
	v_med3_u32 v1, v1, s91, v190
	v_sub_u32_e32 v2, 0x40f, v1
	v_add_u32_e32 v1, 0xfffffdd0, v1
	v_cmp_gt_i32_e32 vcc, 0, v5
	v_med3_f32 v4, v59, v214, v215
	s_nop 0
	v_cndmask_b32_e32 v1, v1, v2, vcc
	v_cmp_eq_f32_e32 vcc, 0, v5
	v_med3_f32 v2, v27, v209, v210
	s_nop 0
	v_cndmask_b32_e32 v1, v1, v0, vcc
	v_cmp_lt_i32_e32 vcc, 17, v160
	s_nop 1
	v_cndmask_b32_e32 v1, v191, v1, vcc
	v_lshl_add_u32 v1, v1, 2, v204
	ds_add_u32 v1, v184
	v_med3_f32 v1, v11, v207, v208
	v_add_f32 v5, v1, v2
	v_add_f32 v6, v3, v4
	v_add_f32 v5, v5, v6
	v_med3_f32 v3, v44, v212, v213
	v_bfe_u32 v1, v5, 20, 11
	v_med3_u32 v1, v1, s91, v190
	v_sub_u32_e32 v2, 0x40f, v1
	v_add_u32_e32 v1, 0xfffffdd0, v1
	v_cmp_gt_i32_e32 vcc, 0, v5
	v_med3_f32 v4, v60, v214, v215
	s_nop 0
	v_cndmask_b32_e32 v1, v1, v2, vcc
	v_cmp_eq_f32_e32 vcc, 0, v5
	v_med3_f32 v2, v28, v209, v210
	s_nop 0
	v_cndmask_b32_e32 v1, v1, v0, vcc
	v_cmp_lt_i32_e32 vcc, 18, v160
	s_nop 1
	v_cndmask_b32_e32 v1, v191, v1, vcc
	v_lshl_add_u32 v1, v1, 2, v204
	ds_add_u32 v1, v184
	v_med3_f32 v1, v12, v207, v208
	v_add_f32 v5, v1, v2
	v_add_f32 v6, v3, v4
	v_add_f32 v5, v5, v6
	v_med3_f32 v3, v45, v212, v213
	v_bfe_u32 v1, v5, 20, 11
	v_med3_u32 v1, v1, s91, v190
	v_sub_u32_e32 v2, 0x40f, v1
	v_add_u32_e32 v1, 0xfffffdd0, v1
	v_cmp_gt_i32_e32 vcc, 0, v5
	v_med3_f32 v4, v61, v214, v215
	s_nop 0
	v_cndmask_b32_e32 v1, v1, v2, vcc
	v_cmp_eq_f32_e32 vcc, 0, v5
	v_med3_f32 v2, v29, v209, v210
	s_nop 0
	v_cndmask_b32_e32 v1, v1, v0, vcc
	v_cmp_lt_i32_e32 vcc, 23, v160
	s_nop 1
	v_cndmask_b32_e32 v1, v191, v1, vcc
	v_lshl_add_u32 v1, v1, 2, v204
	ds_add_u32 v1, v184
	v_med3_f32 v1, v13, v207, v208
	v_add_f32 v5, v1, v2
	v_add_f32 v6, v3, v4
	v_add_f32 v5, v5, v6
	v_med3_f32 v3, v46, v212, v213
	v_bfe_u32 v1, v5, 20, 11
	v_med3_u32 v1, v1, s91, v190
	v_sub_u32_e32 v2, 0x40f, v1
	v_add_u32_e32 v1, 0xfffffdd0, v1
	v_cmp_gt_i32_e32 vcc, 0, v5
	v_med3_f32 v4, v62, v214, v215
	s_nop 0
	v_cndmask_b32_e32 v1, v1, v2, vcc
	v_cmp_eq_f32_e32 vcc, 0, v5
	v_med3_f32 v2, v30, v209, v210
	s_nop 0
	v_cndmask_b32_e32 v1, v1, v0, vcc
	v_cmp_lt_i32_e32 vcc, 24, v160
	s_nop 1
	v_cndmask_b32_e32 v1, v191, v1, vcc
	v_lshl_add_u32 v1, v1, 2, v204
	ds_add_u32 v1, v184
	v_med3_f32 v1, v14, v207, v208
	v_add_f32 v5, v1, v2
	v_add_f32 v6, v3, v4
	v_add_f32 v5, v5, v6
	v_med3_f32 v3, v31, v209, v210
	v_bfe_u32 v1, v5, 20, 11
	v_med3_u32 v1, v1, s91, v190
	v_sub_u32_e32 v2, 0x40f, v1
	v_add_u32_e32 v1, 0xfffffdd0, v1
	v_cmp_gt_i32_e32 vcc, 0, v5
	v_med3_f32 v4, v47, v212, v213
	s_nop 0
	v_cndmask_b32_e32 v1, v1, v2, vcc
	v_cmp_eq_f32_e32 vcc, 0, v5
	v_med3_f32 v2, v15, v207, v208
	v_med3_f32 v5, v63, v214, v215
	v_cndmask_b32_e32 v1, v1, v0, vcc
	v_cmp_lt_i32_e32 vcc, 25, v160
	s_nop 1
	v_cndmask_b32_e32 v1, v191, v1, vcc
	v_lshl_add_u32 v1, v1, 2, v204
	ds_add_u32 v1, v184
	v_add_f32 v1, v2, v3
	v_add_f32 v6, v4, v5
	v_add_f32 v1, v1, v6

; #define DSA2_LOADK(dst, kt_) do { _Pragma("unroll") for (int s = 0; s < 4; ++s) dst[s] = *(const bf16x8*)(kp + (size_t)(32 * (kt_)) * Y0P + 16 * s); } while (0)
; template <int STAGE>
; __device__ __forceinline__ void pass2(LAS unsigned char* lds, const bf16* kbase, int g, int t0, const bf16x8 (&qf)[4][4], const f32x4 lo4, const f32x4 hi4, int wave, int r, int h2) {
;     ...
;             gtw <<= 4 * h2;
;             { auto rr = __builtin_amdgcn_permlane32_swap(gtw, gtw, false, false); gtw = rr[0] | rr[1]; }
;             if (h2 == 0) gtm[r * HROW + kt] = gtw;
;         }
;     };
;     ...
;     int kt = wave;
;     if (kt <= g) DSA2_LOADK(kf, kt);
;     for (;;) {
;         if (kt > g) break;
;         if (kt + 8 <= g) DSA2_LOADK(kn, kt + 8);
;         if (kt == g) { tile(pg8::BoolC2<false>{}, kt, pg8::BoolC2<true>{}); break; }
;         tile(pg8::BoolC2<false>{}, kt, pg8::BoolC2<false>{});
;         kt += 8;
;         if (kt > g) break;
;         if (kt + 8 <= g) DSA2_LOADK(kf, kt + 8);
.LBB0_834:
.LBB0_835:
	v_lshlrev_b32_e32 v0, v219, v0
	v_mov_b32_e32 v1, v0
	s_nop 1
	v_permlane32_swap_b32_e32 v0, v1
	s_and_saveexec_b64 s[6:7], s[84:85]
	v_or_b32_e32 v0, v0, v1
	v_lshl_add_u32 v1, s0, 2, v217
	ds_write_b32 v1, v0
	s_or_b64 exec, exec, s[6:7]
	s_mov_b64 s[6:7], -1
	s_andn2_b64 vcc, exec, s[4:5]
	s_mov_b64 s[4:5], -1
	s_cbranch_vccnz .LBB0_854
	s_add_i32 s10, s0, 16
	s_cmp_gt_u32 s10, s64
	s_cselect_b64 s[4:5], -1, 0
	s_and_b64 vcc, exec, s[4:5]
	s_cbranch_vccnz .LBB0_840
	s_lshl_b32 s6, s10, 5
	v_mad_u64_u32 v[0:1], s[6:7], s6, v187, v[178:179]
	global_load_dwordx4 v[140:143], v[0:1], off
	global_load_dwordx4 v[136:139], v[0:1], off offset:32
	global_load_dwordx4 v[132:135], v[0:1], off offset:64
	global_load_dwordx4 v[128:131], v[0:1], off offset:96

; __device__ __forceinline__ int crow(int reg, int h) { return (reg & 3) + 8 * (reg >> 2) + 4 * h; }
; template <int STAGE>
; __device__ __forceinline__ void pass2(LAS unsigned char* lds, const bf16* kbase, int g, int t0, const bf16x8 (&qf)[4][4], const f32x4 lo4, const f32x4 hi4, int wave, int r, int h2) {
;     ...
;         f32x16 acc[4];
; #pragma unroll
;         for (int hd = 0; hd < 4; ++hd) {
;             acc[hd] = f32x16{};
; #pragma unroll
;             for (int s = 0; s < 4; ++s) acc[hd] = __builtin_amdgcn_mfma_f32_32x32x16_bf16(WN ? kn[s] : kf[s], qf[hd][s], acc[hd], 0, 0, 0);
;         }
;         const int zi = (8191 - 32 * kt) >> 7;
;         const int lim = tq - 32 * kt - 4 * h2;
;         unsigned gtw = 0u, eqw = 0u;
;         float svq[16];
; #pragma unroll
;         for (int rg = 0; rg < 16; ++rg) {
;             const int c0 = att::crow(rg, 0);
;             float sv = fsum4_s(__builtin_amdgcn_fmed3f(acc[0][rg], lo4.x, hi4.x), __builtin_amdgcn_fmed3f(acc[1][rg], lo4.y, hi4.y),
;                                __builtin_amdgcn_fmed3f(acc[2][rg], lo4.z, hi4.z), __builtin_amdgcn_fmed3f(acc[3][rg], lo4.w, hi4.w));
;             const int b = bin2(sv, zi);
;             const bool valid = !DIAG || c0 <= lim;
;             if (STAGE == 0) {
;                 atomicAdd((unsigned*)&hist[r * HROW2 + (valid ? b : NB2)], 1u);
;             } else {
;                 if (valid && b > tb) gtw |= 1u << c0;
;                 if (valid && b == tb) eqw |= 1u << c0;
;                 svq[rg] = sv;
;     ...
;         if (kt == g) { tile(pg8::BoolC2<true>{}, kt, pg8::BoolC2<true>{}); break; }
;         tile(pg8::BoolC2<true>{}, kt, pg8::BoolC2<false>{});
;         kt += 8;
.LBB0_854:
	s_mov_b64 s[8:9], 0
	s_mov_b32 s0, s10
	s_and_b64 vcc, exec, s[4:5]
	s_cbranch_vccnz .LBB0_856
.LBB0_855:
	s_branch .LBB0_824
.LBB0_856:
	s_mov_b64 s[94:95], -1
	s_mov_b64 s[4:5], 0
	s_and_b64 vcc, exec, s[8:9]
	s_cbranch_vccnz .LBB0_867
	s_xor_b64 s[0:1], s[6:7], -1
	s_mov_b64 s[94:95], 0
	s_and_b64 vcc, exec, s[0:1]
	s_cbranch_vccz .LBB0_867
	s_waitcnt vmcnt(3)
	v_mfma_f32_32x32x16_bf16 v[16:31], v[156:159], v[80:83], 0
	s_lshr_b32 s0, s64, 2
	s_sub_i32 s0, 0x10f, s0
	v_mfma_f32_32x32x16_bf16 v[0:15], v[156:159], v[64:67], 0
	v_mfma_f32_32x32x16_bf16 v[32:47], v[156:159], v[96:99], 0
	v_mfma_f32_32x32x16_bf16 v[48:63], v[156:159], v[112:115], 0
	s_waitcnt vmcnt(2)
	v_mfma_f32_32x32x16_bf16 v[16:31], v[152:155], v[84:87], v[16:31]
	v_mfma_f32_32x32x16_bf16 v[0:15], v[152:155], v[68:71], v[0:15]
	v_mfma_f32_32x32x16_bf16 v[32:47], v[152:155], v[100:103], v[32:47]
	v_mfma_f32_32x32x16_bf16 v[48:63], v[152:155], v[116:119], v[48:63]
	s_waitcnt vmcnt(1)
	v_mfma_f32_32x32x16_bf16 v[16:31], v[148:151], v[88:91], v[16:31]
	v_mfma_f32_32x32x16_bf16 v[0:15], v[148:151], v[72:75], v[0:15]
	v_mfma_f32_32x32x16_bf16 v[32:47], v[148:151], v[104:107], v[32:47]
	v_mfma_f32_32x32x16_bf16 v[48:63], v[148:151], v[120:123], v[48:63]
	v_sub_u32_e32 v148, v211, v219
	v_subrev_u32_e32 v148, s41, v148
	v_cmp_lt_i32_e64 s[4:5], -1, v148
	v_cmp_gt_i32_e64 s[6:7], 1, v148
	v_cmp_gt_i32_e64 s[8:9], 2, v148
	v_cmp_gt_i32_e64 s[10:11], 3, v148
	v_cmp_gt_i32_e64 s[12:13], 8, v148
	s_waitcnt vmcnt(0)
	v_mfma_f32_32x32x16_bf16 v[16:31], v[144:147], v[92:95], v[16:31]
	v_cmp_gt_i32_e64 s[14:15], 9, v148
	v_cmp_gt_i32_e64 s[16:17], 10, v148
	v_cmp_gt_i32_e64 s[18:19], 11, v148
	v_cmp_gt_i32_e64 s[20:21], 16, v148
	v_cmp_gt_i32_e64 s[22:23], 17, v148
	v_cmp_gt_i32_e64 s[24:25], 18, v148
	v_cmp_gt_i32_e64 s[26:27], 19, v148
	v_mfma_f32_32x32x16_bf16 v[0:15], v[144:147], v[76:79], v[0:15]
	s_nop 3
	v_med3_f32 v16, v16, v209, v210
	v_med3_f32 v17, v17, v209, v210
	v_med3_f32 v18, v18, v209, v210
	v_med3_f32 v19, v19, v209, v210
	v_med3_f32 v20, v20, v209, v210
	v_med3_f32 v21, v21, v209, v210
	v_cmp_gt_i32_e64 s[28:29], 24, v148
	v_mfma_f32_32x32x16_bf16 v[32:47], v[144:147], v[108:111], v[32:47]
	v_med3_f32 v149, v0, v207, v208
	v_med3_f32 v4, v4, v207, v208
	v_med3_f32 v5, v5, v207, v208
	v_med3_f32 v6, v6, v207, v208
	v_med3_f32 v7, v7, v207, v208
	v_med3_f32 v8, v8, v207, v208
	v_med3_f32 v9, v9, v207, v208
	v_mfma_f32_32x32x16_bf16 v[48:63], v[144:147], v[124:127], v[48:63]
	s_nop 3
	v_med3_f32 v32, v32, v212, v213
	v_med3_f32 v33, v33, v212, v213
	v_med3_f32 v34, v34, v212, v213
	v_med3_f32 v35, v35, v212, v213
	v_med3_f32 v10, v10, v207, v208
	v_med3_f32 v11, v11, v207, v208
	v_med3_f32 v12, v12, v207, v208
	s_nop 0
	v_med3_f32 v48, v48, v214, v215
	v_add_f32 v0, v149, v16
	v_add_f32 v144, v32, v48
	v_add_f32 v0, v0, v144
	v_mov_b32_e32 v48, s0
	v_bfe_u32 v16, v0, 20, 11
	v_med3_u32 v16, v16, s91, v190
	v_sub_u32_e32 v32, 0x40f, v16
	v_add_u32_e32 v16, 0xfffffdd0, v16
	v_cmp_gt_i32_e32 vcc, 0, v0
	v_med3_f32 v144, v1, v207, v208
	v_med3_f32 v49, v49, v214, v215
	v_cndmask_b32_e32 v16, v16, v32, vcc
	v_cmp_eq_f32_e32 vcc, 0, v0
	v_add_f32 v1, v144, v17
	v_add_f32 v145, v33, v49
	v_add_f32 v1, v1, v145
	v_med3_f32 v49, v50, v214, v215
	v_bfe_u32 v17, v1, 20, 11
	v_cndmask_b32_e32 v16, v16, v48, vcc
	s_waitcnt lgkmcnt(0)
	v_cmp_eq_u32_e32 vcc, v16, v222
	v_med3_u32 v17, v17, s91, v190
	s_and_b64 s[0:1], s[4:5], vcc
	v_sub_u32_e32 v33, 0x40f, v17
	v_add_u32_e32 v17, 0xfffffdd0, v17
	v_cmp_gt_i32_e32 vcc, 0, v1
	v_cndmask_b32_e64 v32, 0, 1, s[0:1]
	v_med3_f32 v13, v13, v207, v208
	v_cndmask_b32_e32 v17, v17, v33, vcc
	v_cmp_eq_f32_e32 vcc, 0, v1
	v_cmp_gt_i32_e64 s[30:31], 25, v148
	v_med3_f32 v14, v14, v207, v208
	v_cndmask_b32_e32 v17, v17, v48, vcc
	v_cmp_eq_u32_e32 vcc, v17, v222
	v_med3_f32 v15, v15, v207, v208
	v_cmp_gt_i32_e64 s[34:35], 26, v148
	v_cndmask_b32_e64 v33, 0, 2, vcc
	v_cndmask_b32_e64 v33, v33, 0, s[6:7]
	v_or_b32_e32 v32, v33, v32
	v_med3_f32 v33, v2, v207, v208
	v_add_f32 v2, v33, v18
	v_add_f32 v50, v34, v49
	v_add_f32 v2, v2, v50
	v_med3_f32 v34, v3, v207, v208
	v_bfe_u32 v18, v2, 20, 11
	v_med3_u32 v18, v18, s91, v190
	v_sub_u32_e32 v33, 0x40f, v18
	v_add_u32_e32 v18, 0xfffffdd0, v18
	v_cmp_gt_i32_e32 vcc, 0, v2
	v_med3_f32 v49, v51, v214, v215
	v_add_f32 v3, v34, v19
	v_add_f32 v50, v35, v49
	v_add_f32 v3, v3, v50
	v_med3_f32 v35, v52, v214, v215
	v_cndmask_b32_e32 v18, v18, v33, vcc
	v_cmp_eq_f32_e32 vcc, 0, v2
	v_bfe_u32 v19, v3, 20, 11
	v_med3_u32 v19, v19, s91, v190
	v_cndmask_b32_e32 v18, v18, v48, vcc
	v_cmp_eq_u32_e32 vcc, v18, v222
	v_sub_u32_e32 v34, 0x40f, v19
	v_add_u32_e32 v19, 0xfffffdd0, v19
	v_cndmask_b32_e64 v33, 0, 4, vcc
	v_cmp_gt_i32_e32 vcc, 0, v3
	v_cndmask_b32_e64 v33, v33, 0, s[8:9]
	v_cmp_gt_i32_e64 s[36:37], 27, v148
	v_cndmask_b32_e32 v19, v19, v34, vcc
	v_cmp_eq_f32_e32 vcc, 0, v3
	s_xor_b32 s0, s41, 0x1fff
	s_nop 0
	v_cndmask_b32_e32 v19, v19, v48, vcc
	v_cmp_eq_u32_e32 vcc, v19, v222
	s_nop 1
	v_cndmask_b32_e64 v34, 0, 8, vcc
	v_cndmask_b32_e64 v34, v34, 0, s[10:11]
	v_or3_b32 v34, v32, v33, v34
	v_med3_f32 v33, v36, v212, v213
	v_add_f32 v32, v4, v20
	v_add_f32 v36, v33, v35
	v_add_f32 v32, v32, v36
	v_med3_f32 v35, v37, v212, v213
	v_bfe_u32 v4, v32, 20, 11
	v_med3_u32 v4, v4, s91, v190
	v_sub_u32_e32 v20, 0x40f, v4
	v_add_u32_e32 v4, 0xfffffdd0, v4
	v_cmp_gt_i32_e32 vcc, 0, v32
	v_med3_f32 v36, v53, v214, v215
	v_add_f32 v33, v5, v21
	v_add_f32 v37, v35, v36
	v_add_f32 v33, v33, v37
	v_med3_f32 v35, v54, v214, v215
	v_cndmask_b32_e32 v4, v4, v20, vcc
	v_cmp_eq_f32_e32 vcc, 0, v32
	v_bfe_u32 v5, v33, 20, 11
; #define LAS __attribute__((address_space(3)))
; __device__ __forceinline__ int crow(int reg, int h) { return (reg & 3) + 8 * (reg >> 2) + 4 * h; }
; template <int STAGE>
; __device__ __forceinline__ void pass2(LAS unsigned char* lds, const bf16* kbase, int g, int t0, const bf16x8 (&qf)[4][4], const f32x4 lo4, const f32x4 hi4, int wave, int r, int h2) {
;     ...
;         for (int rg = 0; rg < 16; ++rg) {
;             const int c0 = att::crow(rg, 0);
;             float sv = fsum4_s(__builtin_amdgcn_fmed3f(acc[0][rg], lo4.x, hi4.x), __builtin_amdgcn_fmed3f(acc[1][rg], lo4.y, hi4.y),
;                                __builtin_amdgcn_fmed3f(acc[2][rg], lo4.z, hi4.z), __builtin_amdgcn_fmed3f(acc[3][rg], lo4.w, hi4.w));
;             const int b = bin2(sv, zi);
;             const bool valid = !DIAG || c0 <= lim;
;             if (STAGE == 0) {
;                 atomicAdd((unsigned*)&hist[r * HROW2 + (valid ? b : NB2)], 1u);
;             } else {
;                 if (valid && b > tb) gtw |= 1u << c0;
;                 if (valid && b == tb) eqw |= 1u << c0;
;                 svq[rg] = sv;
;             }
;         }
;         if (STAGE == 1) {
;             LAS unsigned char* st = lds + OFF2_SV + wave * 4096 + (r + 32 * h2) * 16;
; #pragma unroll
;             for (int q = 0; q < 4; ++q) *(LAS f32x4*)(st + q * 1024) = (f32x4){svq[4 * q], svq[4 * q + 1], svq[4 * q + 2], svq[4 * q + 3]};
	v_med3_u32 v5, v5, s91, v190
	v_cndmask_b32_e32 v4, v4, v48, vcc
	v_cmp_eq_u32_e32 vcc, v4, v222
	v_sub_u32_e32 v21, 0x40f, v5
	v_add_u32_e32 v5, 0xfffffdd0, v5
	v_cndmask_b32_e32 v20, 0, v186, vcc
	v_cmp_gt_i32_e32 vcc, 0, v33
	v_cndmask_b32_e64 v20, v20, 0, s[12:13]
	s_nop 0
	v_cndmask_b32_e32 v5, v5, v21, vcc
	v_cmp_eq_f32_e32 vcc, 0, v33
	s_nop 1
	v_cndmask_b32_e32 v5, v5, v48, vcc
	v_cmp_eq_u32_e32 vcc, v5, v222
	s_nop 1
	v_cndmask_b32_e32 v21, 0, v193, vcc
	v_cndmask_b32_e64 v21, v21, 0, s[14:15]
	v_or3_b32 v20, v34, v20, v21
	v_med3_f32 v21, v22, v209, v210
	v_med3_f32 v22, v38, v212, v213
	v_add_f32 v34, v6, v21
	v_add_f32 v36, v22, v35
	v_add_f32 v34, v34, v36
	v_med3_f32 v22, v23, v209, v210
	v_bfe_u32 v6, v34, 20, 11
	v_med3_u32 v6, v6, s91, v190
	v_sub_u32_e32 v21, 0x40f, v6
	v_add_u32_e32 v6, 0xfffffdd0, v6
	v_cmp_gt_i32_e32 vcc, 0, v34
	v_med3_f32 v23, v39, v212, v213
	v_med3_f32 v36, v55, v214, v215
	v_cndmask_b32_e32 v6, v6, v21, vcc
	v_cmp_eq_f32_e32 vcc, 0, v34
	v_add_f32 v35, v7, v22
	v_add_f32 v37, v23, v36
	v_add_f32 v35, v35, v37
	v_med3_f32 v23, v40, v212, v213
	v_bfe_u32 v7, v35, 20, 11
	v_cndmask_b32_e32 v6, v6, v48, vcc
	v_cmp_eq_u32_e32 vcc, v6, v222
	v_med3_u32 v7, v7, s91, v190
	v_sub_u32_e32 v22, 0x40f, v7
	v_cndmask_b32_e32 v21, 0, v194, vcc
	v_add_u32_e32 v7, 0xfffffdd0, v7
	v_cmp_gt_i32_e32 vcc, 0, v35
	v_cndmask_b32_e64 v21, v21, 0, s[16:17]
	s_nop 0
	v_cndmask_b32_e32 v7, v7, v22, vcc
	v_cmp_eq_f32_e32 vcc, 0, v35
	s_nop 1
	v_cndmask_b32_e32 v7, v7, v48, vcc
	v_cmp_eq_u32_e32 vcc, v7, v222
	s_nop 1
	v_cndmask_b32_e32 v22, 0, v195, vcc
	v_cndmask_b32_e64 v22, v22, 0, s[18:19]
	v_or3_b32 v20, v20, v21, v22
	v_med3_f32 v21, v24, v209, v210
	v_med3_f32 v24, v56, v214, v215
	v_add_f32 v22, v8, v21
	v_add_f32 v36, v23, v24
	v_add_f32 v22, v22, v36
	v_med3_f32 v24, v25, v209, v210
	v_bfe_u32 v8, v22, 20, 11
	v_med3_u32 v8, v8, s91, v190
	v_sub_u32_e32 v21, 0x40f, v8
	v_add_u32_e32 v8, 0xfffffdd0, v8
	v_cmp_gt_i32_e32 vcc, 0, v22
	v_med3_f32 v25, v41, v212, v213
	v_med3_f32 v36, v57, v214, v215
	v_cndmask_b32_e32 v8, v8, v21, vcc
	v_cmp_eq_f32_e32 vcc, 0, v22
	v_add_f32 v23, v9, v24
	v_add_f32 v37, v25, v36
	v_add_f32 v23, v23, v37
	v_med3_f32 v25, v42, v212, v213
	v_bfe_u32 v9, v23, 20, 11
	v_cndmask_b32_e32 v8, v8, v48, vcc
	v_cmp_eq_u32_e32 vcc, v8, v222
	v_med3_u32 v9, v9, s91, v190
	v_sub_u32_e32 v24, 0x40f, v9
	v_cndmask_b32_e32 v21, 0, v196, vcc
	v_add_u32_e32 v9, 0xfffffdd0, v9
	v_cmp_gt_i32_e32 vcc, 0, v23
	v_cndmask_b32_e64 v21, v21, 0, s[20:21]
	s_nop 0
	v_cndmask_b32_e32 v9, v9, v24, vcc
	v_cmp_eq_f32_e32 vcc, 0, v23
	s_nop 1
	v_cndmask_b32_e32 v9, v9, v48, vcc
	v_cmp_eq_u32_e32 vcc, v9, v222
	s_nop 1
	v_cndmask_b32_e32 v24, 0, v197, vcc
	v_cndmask_b32_e64 v24, v24, 0, s[22:23]
	v_or3_b32 v20, v20, v21, v24
	v_med3_f32 v21, v26, v209, v210
	v_med3_f32 v26, v58, v214, v215
	v_add_f32 v24, v10, v21
	v_add_f32 v36, v25, v26
	v_add_f32 v24, v24, v36
	v_med3_f32 v26, v27, v209, v210
	v_bfe_u32 v10, v24, 20, 11
	v_med3_u32 v10, v10, s91, v190
	v_sub_u32_e32 v21, 0x40f, v10
	v_add_u32_e32 v10, 0xfffffdd0, v10
	v_cmp_gt_i32_e32 vcc, 0, v24
	v_med3_f32 v27, v43, v212, v213
	v_med3_f32 v36, v59, v214, v215
	v_cndmask_b32_e32 v10, v10, v21, vcc
	v_cmp_eq_f32_e32 vcc, 0, v24
	v_add_f32 v25, v11, v26
	v_add_f32 v37, v27, v36
	v_add_f32 v25, v25, v37
	v_med3_f32 v27, v44, v212, v213
	v_bfe_u32 v11, v25, 20, 11
	v_cndmask_b32_e32 v10, v10, v48, vcc
	v_cmp_eq_u32_e32 vcc, v10, v222
	v_med3_u32 v11, v11, s91, v190
	v_sub_u32_e32 v26, 0x40f, v11
	v_cndmask_b32_e32 v21, 0, v198, vcc
	v_add_u32_e32 v11, 0xfffffdd0, v11
	v_cmp_gt_i32_e32 vcc, 0, v25
	v_cndmask_b32_e64 v21, v21, 0, s[24:25]
	s_nop 0
	v_cndmask_b32_e32 v11, v11, v26, vcc
	v_cmp_eq_f32_e32 vcc, 0, v25
	s_nop 1
	v_cndmask_b32_e32 v11, v11, v48, vcc
	v_cmp_eq_u32_e32 vcc, v11, v222
	s_nop 1
	v_cndmask_b32_e32 v26, 0, v199, vcc
	v_cndmask_b32_e64 v26, v26, 0, s[26:27]
	v_or3_b32 v20, v20, v21, v26
	v_med3_f32 v21, v28, v209, v210
	v_med3_f32 v28, v60, v214, v215
	v_add_f32 v26, v12, v21
	v_add_f32 v36, v27, v28
	v_add_f32 v26, v26, v36
	v_med3_f32 v28, v29, v209, v210
	v_bfe_u32 v12, v26, 20, 11
	v_med3_u32 v12, v12, s91, v190
	v_sub_u32_e32 v21, 0x40f, v12
	v_add_u32_e32 v12, 0xfffffdd0, v12
	v_cmp_gt_i32_e32 vcc, 0, v26
	v_med3_f32 v29, v45, v212, v213
	v_med3_f32 v36, v61, v214, v215
	v_cndmask_b32_e32 v12, v12, v21, vcc
	v_cmp_eq_f32_e32 vcc, 0, v26
	v_add_f32 v27, v13, v28
	v_add_f32 v37, v29, v36
	v_add_f32 v27, v27, v37
	v_med3_f32 v29, v46, v212, v213
	v_bfe_u32 v13, v27, 20, 11
	v_cndmask_b32_e32 v12, v12, v48, vcc
	v_cmp_eq_u32_e32 vcc, v12, v222
	v_med3_u32 v13, v13, s91, v190
	v_sub_u32_e32 v28, 0x40f, v13
	v_cndmask_b32_e32 v21, 0, v200, vcc
	v_add_u32_e32 v13, 0xfffffdd0, v13
	v_cmp_gt_i32_e32 vcc, 0, v27
	v_cndmask_b32_e64 v21, v21, 0, s[28:29]
	s_nop 0
	v_cndmask_b32_e32 v13, v13, v28, vcc
	v_cmp_eq_f32_e32 vcc, 0, v27
	s_nop 1
	v_cndmask_b32_e32 v13, v13, v48, vcc
	v_cmp_eq_u32_e32 vcc, v13, v222
	s_nop 1
	v_cndmask_b32_e32 v28, 0, v201, vcc
	v_cndmask_b32_e64 v28, v28, 0, s[30:31]
	v_or3_b32 v20, v20, v21, v28
	v_med3_f32 v21, v30, v209, v210
	v_med3_f32 v30, v62, v214, v215
	v_add_f32 v28, v14, v21
	v_add_f32 v36, v29, v30
	v_add_f32 v28, v28, v36
	v_med3_f32 v30, v31, v209, v210
	v_bfe_u32 v14, v28, 20, 11
	v_med3_u32 v14, v14, s91, v190
	v_sub_u32_e32 v21, 0x40f, v14
	v_add_u32_e32 v14, 0xfffffdd0, v14
	v_cmp_gt_i32_e32 vcc, 0, v28
	v_med3_f32 v31, v47, v212, v213
	v_med3_f32 v36, v63, v214, v215
	v_cndmask_b32_e32 v14, v14, v21, vcc
	v_cmp_eq_f32_e32 vcc, 0, v28
	v_add_f32 v29, v15, v30
	v_add_f32 v37, v31, v36
	v_add_f32 v29, v29, v37
	ds_write_b128 v223, v[0:3]
	ds_write_b128 v223, v[32:35] offset:1024
	ds_write_b128 v223, v[22:25] offset:2048
	ds_write_b128 v223, v[26:29] offset:3072
	v_cndmask_b32_e32 v14, v14, v48, vcc
	v_bfe_u32 v15, v29, 20, 11
	v_cmp_eq_u32_e32 vcc, v14, v222
	v_med3_u32 v15, v15, s91, v190
	v_sub_u32_e32 v30, 0x40f, v15
	v_cndmask_b32_e32 v21, 0, v202, vcc
	v_add_u32_e32 v15, 0xfffffdd0, v15
	v_cmp_gt_i32_e32 vcc, 0, v29
	v_cndmask_b32_e64 v21, v21, 0, s[34:35]
	s_nop 0
	v_cndmask_b32_e32 v15, v15, v30, vcc
	v_cmp_eq_f32_e32 vcc, 0, v29
	s_nop 1
	v_cndmask_b32_e32 v15, v15, v48, vcc
	v_cmp_eq_u32_e32 vcc, v15, v222
	s_nop 1
	v_cndmask_b32_e32 v30, 0, v203, vcc
	v_cndmask_b32_e64 v30, v30, 0, s[36:37]
	v_or3_b32 v20, v20, v21, v30
	s_branch .LBB0_864
